# k_bfinal conversion blocks: non-temporal loads for the read-once fp32 x
# speedup vs baseline: 1.0155x; 1.0014x over previous
.LBB1_69:
	s_and_b64 vcc, exec, s[4:5]
	s_cbranch_vccz .LBB1_112
	s_load_dwordx4 s[4:7], s[0:1], 0x30
	s_lshl_b32 s2, s2, 10
	s_add_i32 s2, s2, 0xfffd8c00
	v_or_b32_e32 v0, s2, v0
	v_lshlrev_b32_e32 v1, 4, v0
	v_lshlrev_b32_e32 v2, 3, v0
	v_cmp_gt_u32_e32 vcc, 0x800, v0
	s_waitcnt lgkmcnt(0)
	global_load_dwordx4 v[4:7], v1, s[4:5] nt
	s_add_u32 s4, s4, 0x180000
	s_addc_u32 s5, s5, 0
	global_load_dwordx4 v[8:11], v1, s[4:5] nt
	s_add_u32 s4, s4, 0x180000
	s_addc_u32 s5, s5, 0
	global_load_dwordx4 v[12:15], v1, s[4:5] nt
	s_add_u32 s4, s4, 0x180000
	s_addc_u32 s5, s5, 0
	global_load_dwordx4 v[16:19], v1, s[4:5] nt
	s_add_u32 s4, s4, 0x180000
	s_addc_u32 s5, s5, 0
	global_load_dwordx4 v[20:23], v1, s[4:5] nt
	s_add_u32 s4, s4, 0x180000
	s_addc_u32 s5, s5, 0
	global_load_dwordx4 v[24:27], v1, s[4:5] nt
	s_add_u32 s4, s4, 0x180000
	s_addc_u32 s5, s5, 0
	global_load_dwordx4 v[28:31], v1, s[4:5] nt
	s_add_u32 s4, s4, 0x180000
	s_addc_u32 s5, s5, 0
	global_load_dwordx4 v[32:35], v1, s[4:5] nt
	s_add_u32 s4, s4, 0x180000
	s_addc_u32 s5, s5, 0
	global_load_dwordx4 v[36:39], v1, s[4:5] nt
	s_add_u32 s4, s4, 0x180000
	s_addc_u32 s5, s5, 0
	global_load_dwordx4 v[40:43], v1, s[4:5] nt
	s_add_u32 s4, s4, 0x180000
	s_addc_u32 s5, s5, 0
	global_load_dwordx4 v[44:47], v1, s[4:5] nt
	s_add_u32 s4, s4, 0x180000
	s_addc_u32 s5, s5, 0
	global_load_dwordx4 v[48:51], v1, s[4:5] nt
	s_add_u32 s4, s4, 0x180000
	s_addc_u32 s5, s5, 0
	global_load_dwordx4 v[52:55], v1, s[4:5] nt
	s_add_u32 s4, s4, 0x180000
	s_addc_u32 s5, s5, 0
	s_and_saveexec_b64 s[8:9], vcc
	global_load_dwordx4 v[56:59], v1, s[4:5] nt
	s_mov_b64 exec, s[8:9]
	s_waitcnt vmcnt(12)
	v_cvt_pk_f16_f32 v60, v4, v5
	v_cvt_pk_f16_f32 v61, v6, v7
	global_store_dwordx2 v2, v[60:61], s[6:7]
	s_add_u32 s6, s6, 0xc0000
	s_addc_u32 s7, s7, 0
	s_waitcnt vmcnt(12)
	v_cvt_pk_f16_f32 v62, v8, v9
	v_cvt_pk_f16_f32 v63, v10, v11
	global_store_dwordx2 v2, v[62:63], s[6:7]
	s_add_u32 s6, s6, 0xc0000
	s_addc_u32 s7, s7, 0
	s_waitcnt vmcnt(12)
	v_cvt_pk_f16_f32 v60, v12, v13
	v_cvt_pk_f16_f32 v61, v14, v15
	global_store_dwordx2 v2, v[60:61], s[6:7]
	s_add_u32 s6, s6, 0xc0000
	s_addc_u32 s7, s7, 0
	s_waitcnt vmcnt(12)
	v_cvt_pk_f16_f32 v62, v16, v17
	v_cvt_pk_f16_f32 v63, v18, v19
	global_store_dwordx2 v2, v[62:63], s[6:7]
	s_add_u32 s6, s6, 0xc0000
	s_addc_u32 s7, s7, 0
	s_waitcnt vmcnt(12)
	v_cvt_pk_f16_f32 v60, v20, v21
	v_cvt_pk_f16_f32 v61, v22, v23
	global_store_dwordx2 v2, v[60:61], s[6:7]
	s_add_u32 s6, s6, 0xc0000
	s_addc_u32 s7, s7, 0
	s_waitcnt vmcnt(12)
	v_cvt_pk_f16_f32 v62, v24, v25
	v_cvt_pk_f16_f32 v63, v26, v27
	global_store_dwordx2 v2, v[62:63], s[6:7]
	s_add_u32 s6, s6, 0xc0000
	s_addc_u32 s7, s7, 0
	s_waitcnt vmcnt(12)
	v_cvt_pk_f16_f32 v60, v28, v29
	v_cvt_pk_f16_f32 v61, v30, v31
	global_store_dwordx2 v2, v[60:61], s[6:7]
	s_add_u32 s6, s6, 0xc0000
	s_addc_u32 s7, s7, 0
	s_waitcnt vmcnt(12)
	v_cvt_pk_f16_f32 v62, v32, v33
	v_cvt_pk_f16_f32 v63, v34, v35
	global_store_dwordx2 v2, v[62:63], s[6:7]
	s_add_u32 s6, s6, 0xc0000
	s_addc_u32 s7, s7, 0
	s_waitcnt vmcnt(12)
	v_cvt_pk_f16_f32 v60, v36, v37
	v_cvt_pk_f16_f32 v61, v38, v39
	global_store_dwordx2 v2, v[60:61], s[6:7]
	s_add_u32 s6, s6, 0xc0000
	s_addc_u32 s7, s7, 0
	s_waitcnt vmcnt(12)
	v_cvt_pk_f16_f32 v62, v40, v41
	v_cvt_pk_f16_f32 v63, v42, v43
	global_store_dwordx2 v2, v[62:63], s[6:7]
	s_add_u32 s6, s6, 0xc0000
	s_addc_u32 s7, s7, 0
	s_waitcnt vmcnt(12)
	v_cvt_pk_f16_f32 v60, v44, v45
	v_cvt_pk_f16_f32 v61, v46, v47
	global_store_dwordx2 v2, v[60:61], s[6:7]
	s_add_u32 s6, s6, 0xc0000
	s_addc_u32 s7, s7, 0
	s_waitcnt vmcnt(12)
	v_cvt_pk_f16_f32 v62, v48, v49
	v_cvt_pk_f16_f32 v63, v50, v51
	global_store_dwordx2 v2, v[62:63], s[6:7]
	s_add_u32 s6, s6, 0xc0000
	s_addc_u32 s7, s7, 0
	s_waitcnt vmcnt(12)
	v_cvt_pk_f16_f32 v60, v52, v53
	v_cvt_pk_f16_f32 v61, v54, v55
	global_store_dwordx2 v2, v[60:61], s[6:7]
	s_add_u32 s6, s6, 0xc0000
	s_addc_u32 s7, s7, 0
	s_and_saveexec_b64 s[8:9], vcc
	s_waitcnt vmcnt(0)
	v_cvt_pk_f16_f32 v62, v56, v57
	v_cvt_pk_f16_f32 v63, v58, v59
	global_store_dwordx2 v2, v[62:63], s[6:7]
